# attention flash loops: tile-list entries (mask / DMA addresses) prefetched one iteration ahead instead of read at the point of use
# baseline (speedup 1.0000x reference)
; #define VM_WAIT() asm volatile("s_waitcnt vmcnt(0)" ::: "memory")
; #define BAR() do { asm volatile("" ::: "memory"); __builtin_amdgcn_s_barrier(); asm volatile("" ::: "memory"); } while (0)
; #define DMA(ti, slot) do { const int _b = __builtin_amdgcn_readfirstlane(list[ti]); int offK[2], offV[2]; dma_offsets(ldk, wid, lane, offK, offV); \
;         dma_tile(K_lds + (slot) * SHM, Kb, (size_t)_b * 64 * ldk, offK, wid); dma_tile(V_lds + (slot) * SHM, Vb, (size_t)_b * 64 * ldk, offV, wid); } while (0)
; template <int MODE> ...
;     ...
;     DMA(0, 0); if (n > 1) DMA(1, 1); if (n > 2) DMA(2, 2);
;     VM_WAIT(); __syncthreads();
;     if (half) BAR();
;     bf16x8 pa0, pa1, pa2, pa3;
;     int buf = 0;
;     for (int i = 0; i < n; ++i) {
;         const int bcur = __builtin_amdgcn_readfirstlane(list[i]);
;         const int pslot = (buf == 0) ? 2 : buf - 1;
;         const int nslot = (buf == 2) ? 0 : buf + 1;
;         if (half == 0 && i + 1 >= 3 && i + 1 < n) DMA(i + 1, nslot);
.LBB0_594:
	s_barrier
	v_add_f32_e32 v84, v84, v85
	v_add_f32_e32 v2, v2, v84
	s_cmp_eq_u32 s18, 2
	s_mov_b32 s26, 2
	s_cbranch_scc1 .LBB0_615
	s_movk_i32 s53, 0x18f
	s_movk_i32 s52, 0x19f
	s_mov_b32 s17, 2
	v_readlane_b32 s27, v245, 34
	s_mov_b32 s28, 2
	v_mov_b32_e32 v211, s27
	v_add_u32_e32 v211, -8, v211
	ds_read_b32 v208, v211
	ds_read_b32 v209, v211 offset:4
	ds_read_b32 v210, v211 offset:8
.LBB0_596:
	s_add_i32 s16, s17, 1
	s_cmp_lg_u32 s17, 2
	s_cselect_b32 s26, s16, 0
	s_and_b64 vcc, exec, s[10:11]
	s_waitcnt lgkmcnt(0)
	v_readfirstlane_b32 s16, v208
	s_cbranch_vccnz .LBB0_599
	s_add_i32 s29, s28, 1
	s_cmp_ge_i32 s29, s18
	s_cbranch_scc1 .LBB0_599
	s_lshl_b32 s29, s26, 14
	v_readfirstlane_b32 s34, v209
	s_ashr_i32 s35, s34, 31
	s_lshl_b64 s[34:35], s[34:35], 14
	s_add_u32 s36, s14, s34
	s_addc_u32 s37, s15, s35
	s_add_i32 s29, s21, s29
	s_add_i32 m0, s29, 0xc000
	v_lshl_add_u64 v[84:85], v[136:137], 1, s[36:37]
	global_load_lds_dwordx4 v[84:85], off
	s_add_i32 m0, s29, 0xc400
	s_add_u32 s34, s19, s34
	v_lshl_add_u64 v[84:85], v[140:141], 1, s[36:37]
	s_addc_u32 s35, s20, s35
	global_load_lds_dwordx4 v[84:85], off
	v_lshl_add_u64 v[84:85], v[138:139], 1, s[34:35]
	s_mov_b32 m0, s29
	s_movk_i32 s37, 0x1af
	global_load_lds_dwordx4 v[84:85], off
	v_lshl_add_u64 v[84:85], v[142:143], 1, s[34:35]
	s_add_i32 m0, s29, 0x400
	s_movk_i32 s36, 0x7f
	global_load_lds_dwordx4 v[84:85], off

; #define VM_WAIT() asm volatile("s_waitcnt vmcnt(0)" ::: "memory")
; #define BAR() do { asm volatile("" ::: "memory"); __builtin_amdgcn_s_barrier(); asm volatile("" ::: "memory"); } while (0)
; #define DMA(ti, slot) do { const int _b = __builtin_amdgcn_readfirstlane(list[ti]); int offK[2], offV[2]; dma_offsets(ldk, wid, lane, offK, offV); \
;         dma_tile(K_lds + (slot) * SHM, Kb, (size_t)_b * 64 * ldk, offK, wid); dma_tile(V_lds + (slot) * SHM, Vb, (size_t)_b * 64 * ldk, offV, wid); } while (0)
; template <int MODE> ...
;     ...
;         if (half == 1) VM_WAIT();
;         BAR();
;         if (half == 1 && i + 2 >= 3 && i + 2 < n) DMA(i + 2, pslot);
;         const int dist0 = (MODE == 0) ? (t - 31 - 1024 * bcur - 64 * hi) : (t - 64 * bcur - 4 * hi);
;         float nbl = -slope2 * (float)dist0;
;         if (MODE == 1) { const unsigned mw = selw[bcur >> 5]; if (!((mw >> (bcur & 31)) & 1u)) nbl = -__builtin_inff(); }
; #pragma unroll
;         for (int r = 0; r < 16; ++r) { const float c0 = ks * (float)((r & 3) + 8 * (r >> 2)), c1 = c0 + 32.f * ks; p0[r] = fmaf(slope2, c0, p0[r]); p1[r] = fmaf(slope2, c1, p1[r]); }
;         if (bcur >= bA || bcur == bB) {
;             const float base = (float)dist0;
; #pragma unroll
;             for (int r = 0; r < 16; ++r) { const float c0 = ks * (float)((r & 3) + 8 * (r >> 2)), c1 = c0 + 32.f * ks; const float d0 = base - c0, d1 = base - c1;
;                 bool v0 = d0 >= 0.f, v1 = d1 >= 0.f;
;                 if (MODE == 2) { v0 = v0 && (d0 < 512.f); v1 = v1 && (d1 < 512.f); }
;                 p0[r] = v0 ? p0[r] : -__builtin_inff(); p1[r] = v1 ? p1[r] : -__builtin_inff(); }
;         }
.LBB0_601:
	s_setprio 0
	s_barrier
	s_and_b64 vcc, exec, s[12:13]
	s_cbranch_vccnz .LBB0_604
	s_add_i32 s29, s28, 2
	s_cmp_ge_i32 s29, s18
	s_cbranch_scc1 .LBB0_604
	v_readfirstlane_b32 s34, v210
	s_ashr_i32 s35, s34, 31
	s_lshl_b64 s[34:35], s[34:35], 14
	s_add_u32 s36, s14, s34
	s_addc_u32 s37, s15, s35
	s_add_i32 s17, s21, s17
	s_add_i32 m0, s17, 0xc000
	v_lshl_add_u64 v[144:145], v[136:137], 1, s[36:37]
	global_load_lds_dwordx4 v[144:145], off
	s_add_i32 m0, s17, 0xc400
	s_add_u32 s34, s19, s34
	v_lshl_add_u64 v[144:145], v[140:141], 1, s[36:37]
	s_addc_u32 s35, s20, s35
	global_load_lds_dwordx4 v[144:145], off
	v_lshl_add_u64 v[144:145], v[138:139], 1, s[34:35]
	s_mov_b32 m0, s17
	s_movk_i32 s37, 0x1af
	global_load_lds_dwordx4 v[144:145], off
	v_lshl_add_u64 v[144:145], v[142:143], 1, s[34:35]
	s_add_i32 m0, s17, 0x400
	s_movk_i32 s36, 0x7f
	global_load_lds_dwordx4 v[144:145], off
.LBB0_604:
	v_mov_b32_e32 v211, s27
	v_add_u32_e32 v211, -4, v211
	ds_read_b32 v208, v211
	ds_read_b32 v209, v211 offset:4
	ds_read_b32 v210, v211 offset:8
	s_mov_b32 s34, 0x43c00000
	s_mov_b32 s35, 0x43c80000
	s_nop 2
	v_pk_fma_f32 v[144:145], v[134:135], s[64:65], v[68:69]
	s_nop 1
	v_pk_fma_f32 v[68:69], v[134:135], s[82:83], v[84:85]
	v_pk_fma_f32 v[84:85], v[134:135], s[60:61], v[70:71]
	v_pk_fma_f32 v[70:71], v[134:135], s[38:39], v[86:87]
	v_pk_fma_f32 v[86:87], v[134:135], s[40:41], v[72:73]
	v_pk_fma_f32 v[72:73], v[134:135], s[42:43], v[88:89]
	v_pk_fma_f32 v[88:89], v[134:135], s[44:45], v[74:75]
	v_pk_fma_f32 v[74:75], v[134:135], s[46:47], v[90:91]
	v_pk_fma_f32 v[90:91], v[134:135], s[48:49], v[76:77]
	v_pk_fma_f32 v[76:77], v[134:135], s[50:51], v[92:93]
	v_pk_fma_f32 v[92:93], v[134:135], s[62:63], v[78:79]
	v_pk_fma_f32 v[78:79], v[134:135], s[58:59], v[94:95]
	v_pk_fma_f32 v[94:95], v[134:135], s[34:35], v[80:81]
	s_mov_b32 s34, 0x44600000
	s_mov_b32 s35, 0x44640000
	v_pk_fma_f32 v[80:81], v[134:135], s[34:35], v[96:97]
	s_mov_b32 s34, 0x43d00000
	s_mov_b32 s35, 0x43d80000
	s_lshl_b32 s17, s16, 10
	v_pk_fma_f32 v[96:97], v[134:135], s[34:35], v[82:83]
	s_mov_b32 s34, 0x44680000
	s_mov_b32 s35, 0x446c0000
	s_cmp_lt_i32 s16, s22
	v_pk_fma_f32 v[82:83], v[134:135], s[34:35], v[98:99]
	s_cselect_b64 s[34:35], -1, 0
	s_cmp_lg_u32 s16, -1
	v_subrev_u32_e32 v175, s17, v179
	s_cselect_b64 s[16:17], -1, 0
	s_and_b64 s[16:17], s[34:35], s[16:17]
	s_and_b64 vcc, exec, s[16:17]
	s_cbranch_vccnz .LBB0_606
	v_cmp_lt_i32_e32 vcc, -1, v175
	s_nop 1
	v_cndmask_b32_e32 v144, v161, v144, vcc
	v_cmp_lt_i32_e32 vcc, 15, v175
	s_nop 1
	v_cndmask_b32_e32 v145, v161, v145, vcc
	v_cmp_lt_i32_e32 vcc, 31, v175
	s_nop 1
	v_cndmask_b32_e32 v84, v161, v84, vcc
	v_cmp_lt_i32_e32 vcc, 47, v175
	s_nop 1
	v_cndmask_b32_e32 v85, v161, v85, vcc
	v_cmp_lt_i32_e32 vcc, s36, v175
	s_nop 1
	v_cndmask_b32_e32 v86, v161, v86, vcc
	v_cmp_lt_i32_e32 vcc, s66, v175
	s_nop 1
	v_cndmask_b32_e32 v87, v161, v87, vcc
	v_cmp_lt_i32_e32 vcc, s77, v175
	s_nop 1
	v_cndmask_b32_e32 v88, v161, v88, vcc
	v_cmp_lt_i32_e32 vcc, s76, v175
	s_nop 1
	v_cndmask_b32_e32 v89, v161, v89, vcc
	v_cmp_lt_i32_e32 vcc, s5, v175
	s_nop 1
	v_cndmask_b32_e32 v90, v161, v90, vcc
	v_cmp_lt_i32_e32 vcc, s4, v175
	s_nop 1
	v_cndmask_b32_e32 v91, v161, v91, vcc
	v_cmp_lt_i32_e32 vcc, s73, v175
	s_nop 1
	v_cndmask_b32_e32 v92, v161, v92, vcc
	v_cmp_lt_i32_e32 vcc, s74, v175
	s_nop 1
	v_cndmask_b32_e32 v93, v161, v93, vcc
	v_cmp_lt_i32_e32 vcc, s54, v175
	s_nop 1
	v_cndmask_b32_e32 v94, v161, v94, vcc
	v_cmp_lt_i32_e32 vcc, s53, v175
	s_nop 1
	v_cndmask_b32_e32 v95, v161, v95, vcc
	v_cmp_lt_i32_e32 vcc, s52, v175
	s_nop 1
	v_cndmask_b32_e32 v96, v161, v96, vcc
	v_cmp_lt_i32_e32 vcc, s37, v175
	s_nop 1
	v_cndmask_b32_e32 v97, v161, v97, vcc
	v_cmp_lt_i32_e32 vcc, s33, v175
	s_nop 1
	v_cndmask_b32_e32 v68, v161, v68, vcc
	v_cmp_lt_i32_e32 vcc, s89, v175
	s_nop 1
	v_cndmask_b32_e32 v69, v161, v69, vcc
	v_cmp_lt_i32_e32 vcc, s88, v175
	s_nop 1
	v_cndmask_b32_e32 v70, v161, v70, vcc
	v_cmp_lt_i32_e32 vcc, s93, v175
	s_nop 1
	v_cndmask_b32_e32 v71, v161, v71, vcc
	v_cmp_lt_i32_e32 vcc, s92, v175
	s_nop 1
	v_cndmask_b32_e32 v72, v161, v72, vcc
	v_cmp_lt_i32_e32 vcc, s87, v175
	s_nop 1
	v_cndmask_b32_e32 v73, v161, v73, vcc
	v_cmp_lt_i32_e32 vcc, s86, v175
	s_nop 1
	v_cndmask_b32_e32 v74, v161, v74, vcc
	v_cmp_lt_i32_e32 vcc, s0, v175
	s_nop 1
	v_cndmask_b32_e32 v75, v161, v75, vcc
	v_cmp_lt_i32_e32 vcc, s81, v175
	s_nop 1
	v_cndmask_b32_e32 v76, v161, v76, vcc
	v_cmp_lt_i32_e32 vcc, s80, v175
	s_nop 1
	v_cndmask_b32_e32 v77, v161, v77, vcc
	v_cmp_lt_i32_e32 vcc, s79, v175
	s_nop 1
	v_cndmask_b32_e32 v78, v161, v78, vcc
	v_cmp_lt_i32_e32 vcc, s78, v175
	s_nop 1
	v_cndmask_b32_e32 v79, v161, v79, vcc
	v_cmp_lt_i32_e32 vcc, s71, v175
	s_nop 1
	v_cndmask_b32_e32 v80, v161, v80, vcc
	v_cmp_lt_i32_e32 vcc, s70, v175
	s_nop 1
	v_cndmask_b32_e32 v81, v161, v81, vcc
	v_cmp_lt_i32_e32 vcc, s69, v175
	s_nop 1
	v_cndmask_b32_e32 v82, v161, v82, vcc
	v_cmp_lt_i32_e32 vcc, s68, v175
	s_nop 1
	v_cndmask_b32_e32 v83, v161, v83, vcc

; #define VM_WAIT() asm volatile("s_waitcnt vmcnt(0)" ::: "memory")
; #define BAR() do { asm volatile("" ::: "memory"); __builtin_amdgcn_s_barrier(); asm volatile("" ::: "memory"); } while (0)
; #define DMA(ti, slot) do { const int _b = __builtin_amdgcn_readfirstlane(list[ti]); int offK[2], offV[2]; dma_offsets(ldk, wid, lane, offK, offV); \
;         dma_tile(K_lds + (slot) * SHM, Kb, (size_t)_b * 64 * ldk, offK, wid); dma_tile(V_lds + (slot) * SHM, Vb, (size_t)_b * 64 * ldk, offV, wid); } while (0)
; template <int MODE> ...
;     ...
;     DMA(0, 0); if (n > 1) DMA(1, 1); if (n > 2) DMA(2, 2);
;     VM_WAIT(); __syncthreads();
;     if (half) BAR();
;     bf16x8 pa0, pa1, pa2, pa3;
;     int buf = 0;
;     for (int i = 0; i < n; ++i) {
;         const int bcur = __builtin_amdgcn_readfirstlane(list[i]);
;         const int pslot = (buf == 0) ? 2 : buf - 1;
;         const int nslot = (buf == 2) ? 0 : buf + 1;
;         if (half == 0 && i + 1 >= 3 && i + 1 < n) DMA(i + 1, nslot);
.LBB0_770:
	s_barrier
	v_add_f32_e32 v84, v84, v85
	v_add_f32_e32 v2, v2, v84
	s_cmp_eq_u32 s6, 2
	s_mov_b32 s16, 2
	s_cbranch_scc1 .LBB0_791
	s_mov_b32 s13, 2
	v_readlane_b32 s7, v245, 43
	s_mov_b32 s17, 2
	v_mov_b32_e32 v211, s7
	v_add_u32_e32 v211, -8, v211
	ds_read_b32 v208, v211
	ds_read_b32 v209, v211 offset:4
	ds_read_b32 v210, v211 offset:8
.LBB0_772:
	s_add_i32 s12, s13, 1
	s_cmp_lg_u32 s13, 2
	s_cselect_b32 s16, s12, 0
	s_and_b64 vcc, exec, s[8:9]
	s_waitcnt lgkmcnt(0)
	v_readfirstlane_b32 s12, v208
	s_cbranch_vccnz .LBB0_775
	s_add_i32 s18, s17, 1
	s_cmp_ge_i32 s18, s6
	s_cbranch_scc1 .LBB0_775
	s_lshl_b32 s20, s16, 14
	s_mov_b64 s[34:35], 0x800
	v_readfirstlane_b32 s18, v209
	s_mul_hi_i32 s19, s18, 0x1e8000
	s_mul_i32 s18, s18, 0x1e8000
	s_add_u32 s18, s14, s18
	s_addc_u32 s19, s15, s19
	s_add_i32 s20, s90, s20
	v_lshl_add_u64 v[84:85], v[152:153], 1, s[18:19]
	s_add_i32 m0, s20, 0xc000
	v_lshl_add_u64 v[84:85], v[84:85], 0, s[34:35]
	global_load_lds_dwordx4 v[84:85], off
	v_lshl_add_u64 v[84:85], v[156:157], 1, s[18:19]
	v_lshl_add_u64 v[84:85], v[84:85], 0, s[34:35]
	s_add_i32 m0, s20, 0xc400
	s_mov_b64 s[34:35], 0xc00
	global_load_lds_dwordx4 v[84:85], off
	v_lshl_add_u64 v[84:85], v[154:155], 1, s[18:19]
	v_lshl_add_u64 v[84:85], v[84:85], 0, s[34:35]
	s_mov_b32 m0, s20
	s_nop 0
	global_load_lds_dwordx4 v[84:85], off
	v_lshl_add_u64 v[84:85], v[158:159], 1, s[18:19]
	v_lshl_add_u64 v[84:85], v[84:85], 0, s[34:35]
	s_add_i32 m0, s20, 0x400
	s_nop 0
	global_load_lds_dwordx4 v[84:85], off

; #define VM_WAIT() asm volatile("s_waitcnt vmcnt(0)" ::: "memory")
; #define BAR() do { asm volatile("" ::: "memory"); __builtin_amdgcn_s_barrier(); asm volatile("" ::: "memory"); } while (0)
; #define DMA(ti, slot) do { const int _b = __builtin_amdgcn_readfirstlane(list[ti]); int offK[2], offV[2]; dma_offsets(ldk, wid, lane, offK, offV); \
;         dma_tile(K_lds + (slot) * SHM, Kb, (size_t)_b * 64 * ldk, offK, wid); dma_tile(V_lds + (slot) * SHM, Vb, (size_t)_b * 64 * ldk, offV, wid); } while (0)
; template <int MODE> ...
;     ...
;         if (half == 1) VM_WAIT();
;         BAR();
;         if (half == 1 && i + 2 >= 3 && i + 2 < n) DMA(i + 2, pslot);
;         const int dist0 = (MODE == 0) ? (t - 31 - 1024 * bcur - 64 * hi) : (t - 64 * bcur - 4 * hi);
;         float nbl = -slope2 * (float)dist0;
;         if (MODE == 1) { const unsigned mw = selw[bcur >> 5]; if (!((mw >> (bcur & 31)) & 1u)) nbl = -__builtin_inff(); }
; #pragma unroll
;         for (int r = 0; r < 16; ++r) { const float c0 = ks * (float)((r & 3) + 8 * (r >> 2)), c1 = c0 + 32.f * ks; p0[r] = fmaf(slope2, c0, p0[r]); p1[r] = fmaf(slope2, c1, p1[r]); }
;         if (bcur >= bA || bcur == bB) {
;             const float base = (float)dist0;
; #pragma unroll
;             for (int r = 0; r < 16; ++r) { const float c0 = ks * (float)((r & 3) + 8 * (r >> 2)), c1 = c0 + 32.f * ks; const float d0 = base - c0, d1 = base - c1;
;                 bool v0 = d0 >= 0.f, v1 = d1 >= 0.f;
;                 if (MODE == 2) { v0 = v0 && (d0 < 512.f); v1 = v1 && (d1 < 512.f); }
;                 p0[r] = v0 ? p0[r] : -__builtin_inff(); p1[r] = v1 ? p1[r] : -__builtin_inff(); }
;         }
.LBB0_777:
	s_setprio 0
	s_barrier
	s_and_b64 vcc, exec, s[10:11]
	s_cbranch_vccnz .LBB0_780
	s_add_i32 s18, s17, 2
	s_cmp_ge_i32 s18, s6
	s_cbranch_scc1 .LBB0_780
	s_mov_b64 s[20:21], 0x800
	v_readfirstlane_b32 s18, v210
	s_mul_hi_i32 s19, s18, 0x1e8000
	s_mul_i32 s18, s18, 0x1e8000
	s_add_u32 s18, s14, s18
	s_addc_u32 s19, s15, s19
	s_add_i32 s13, s90, s13
	v_lshl_add_u64 v[188:189], v[152:153], 1, s[18:19]
	s_add_i32 m0, s13, 0xc000
	v_lshl_add_u64 v[188:189], v[188:189], 0, s[20:21]
	global_load_lds_dwordx4 v[188:189], off
	v_lshl_add_u64 v[188:189], v[156:157], 1, s[18:19]
	v_lshl_add_u64 v[188:189], v[188:189], 0, s[20:21]
	s_add_i32 m0, s13, 0xc400
	s_mov_b64 s[20:21], 0xc00
	global_load_lds_dwordx4 v[188:189], off
	v_lshl_add_u64 v[188:189], v[154:155], 1, s[18:19]
	v_lshl_add_u64 v[188:189], v[188:189], 0, s[20:21]
	s_mov_b32 m0, s13
	s_nop 0
	global_load_lds_dwordx4 v[188:189], off
	v_lshl_add_u64 v[188:189], v[158:159], 1, s[18:19]
	v_lshl_add_u64 v[188:189], v[188:189], 0, s[20:21]
	s_add_i32 m0, s13, 0x400
	s_nop 0
	global_load_lds_dwordx4 v[188:189], off
.LBB0_780:
	v_mov_b32_e32 v211, s7
	v_add_u32_e32 v211, -4, v211
	ds_read_b32 v208, v211
	ds_read_b32 v209, v211 offset:4
	ds_read_b32 v210, v211 offset:8
	v_lshl_add_u32 v188, s12, 6, v140
	s_ashr_i32 s13, s12, 5
	v_sub_u32_e32 v190, v166, v188
	v_lshl_add_u32 v188, s13, 2, v172
	ds_read_b32 v191, v188
	s_cmp_lt_i32 s12, s67
	s_cselect_b64 s[18:19], -1, 0
	s_cmp_lg_u32 s12, -1
	s_cselect_b64 s[20:21], -1, 0
	s_mov_b32 s84, s60
	s_mov_b32 s94, s65
	s_mov_b32 s74, s61
	s_and_b64 s[18:19], s[18:19], s[20:21]
	v_fma_f32 v189, 0, v134, v68
	v_add_f32_e32 v188, v134, v69
	v_pk_fma_f32 v[68:69], v[134:135], s[84:85], v[84:85]
	v_pk_fma_f32 v[84:85], v[134:135], s[22:23], v[70:71]
	v_pk_fma_f32 v[70:71], v[134:135], s[24:25], v[86:87]
	v_pk_fma_f32 v[86:87], v[134:135], s[56:57], v[72:73]
	v_pk_fma_f32 v[72:73], v[134:135], s[26:27], v[88:89]
	v_pk_fma_f32 v[88:89], v[134:135], s[28:29], v[74:75]
	v_pk_fma_f32 v[74:75], v[134:135], s[36:37], v[90:91]
	v_pk_fma_f32 v[90:91], v[134:135], s[94:95], v[76:77]
	v_pk_fma_f32 v[76:77], v[134:135], s[74:75], v[92:93]
	v_pk_fma_f32 v[92:93], v[134:135], s[38:39], v[78:79]
	v_pk_fma_f32 v[78:79], v[134:135], s[40:41], v[94:95]
	v_pk_fma_f32 v[94:95], v[134:135], s[42:43], v[80:81]
	v_pk_fma_f32 v[80:81], v[134:135], s[44:45], v[96:97]
	v_pk_fma_f32 v[96:97], v[134:135], s[46:47], v[82:83]
	v_pk_fma_f32 v[82:83], v[134:135], s[48:49], v[98:99]
	s_and_b64 vcc, exec, s[18:19]
	s_cbranch_vccnz .LBB0_782
	v_cmp_lt_i32_e32 vcc, -1, v190
	s_nop 1
	v_cndmask_b32_e32 v189, v161, v189, vcc
	v_cmp_lt_i32_e32 vcc, 0, v190
	s_nop 1
	v_cndmask_b32_e32 v188, v161, v188, vcc
	v_cmp_lt_i32_e32 vcc, 1, v190
	s_nop 1
	v_cndmask_b32_e32 v84, v161, v84, vcc
	v_cmp_lt_i32_e32 vcc, 2, v190
	s_nop 1
	v_cndmask_b32_e32 v85, v161, v85, vcc
	v_cmp_lt_i32_e32 vcc, 7, v190
	s_nop 1
	v_cndmask_b32_e32 v86, v161, v86, vcc
	v_cmp_lt_i32_e32 vcc, 8, v190
	s_nop 1
	v_cndmask_b32_e32 v87, v161, v87, vcc
	v_cmp_lt_i32_e32 vcc, 9, v190
	s_nop 1
	v_cndmask_b32_e32 v88, v161, v88, vcc
	v_cmp_lt_i32_e32 vcc, 10, v190
	s_nop 1
	v_cndmask_b32_e32 v89, v161, v89, vcc
	v_cmp_lt_i32_e32 vcc, 15, v190
	s_nop 1
	v_cndmask_b32_e32 v90, v161, v90, vcc
	v_cmp_lt_i32_e32 vcc, 16, v190
	s_nop 1
	v_cndmask_b32_e32 v91, v161, v91, vcc
	v_cmp_lt_i32_e32 vcc, 17, v190
	s_nop 1
	v_cndmask_b32_e32 v92, v161, v92, vcc
	v_cmp_lt_i32_e32 vcc, 18, v190
	s_nop 1
	v_cndmask_b32_e32 v93, v161, v93, vcc
	v_cmp_lt_i32_e32 vcc, 23, v190
	s_nop 1
	v_cndmask_b32_e32 v94, v161, v94, vcc
	v_cmp_lt_i32_e32 vcc, 24, v190
	s_nop 1
	v_cndmask_b32_e32 v95, v161, v95, vcc
	v_cmp_lt_i32_e32 vcc, 25, v190
	s_nop 1
	v_cndmask_b32_e32 v96, v161, v96, vcc
	v_cmp_lt_i32_e32 vcc, 26, v190
	s_nop 1
	v_cndmask_b32_e32 v97, v161, v97, vcc
	v_cmp_lt_i32_e32 vcc, 31, v190
	s_nop 1
	v_cndmask_b32_e32 v68, v161, v68, vcc
	v_cmp_lt_i32_e32 vcc, 32, v190
	s_nop 1
	v_cndmask_b32_e32 v69, v161, v69, vcc
	v_cmp_lt_i32_e32 vcc, 33, v190
	s_nop 1
	v_cndmask_b32_e32 v70, v161, v70, vcc
	v_cmp_lt_i32_e32 vcc, 34, v190
	s_nop 1
	v_cndmask_b32_e32 v71, v161, v71, vcc
	v_cmp_lt_i32_e32 vcc, 39, v190
	s_nop 1
	v_cndmask_b32_e32 v72, v161, v72, vcc
	v_cmp_lt_i32_e32 vcc, 40, v190
	s_nop 1
	v_cndmask_b32_e32 v73, v161, v73, vcc
	v_cmp_lt_i32_e32 vcc, 41, v190
	s_nop 1
	v_cndmask_b32_e32 v74, v161, v74, vcc
	v_cmp_lt_i32_e32 vcc, 42, v190
	s_nop 1
	v_cndmask_b32_e32 v75, v161, v75, vcc
	v_cmp_lt_i32_e32 vcc, 47, v190
	s_nop 1
	v_cndmask_b32_e32 v76, v161, v76, vcc
	v_cmp_lt_i32_e32 vcc, 48, v190
	s_nop 1
	v_cndmask_b32_e32 v77, v161, v77, vcc
	v_cmp_lt_i32_e32 vcc, 49, v190
	s_nop 1
	v_cndmask_b32_e32 v78, v161, v78, vcc
	v_cmp_lt_i32_e32 vcc, 50, v190
	s_nop 1
	v_cndmask_b32_e32 v79, v161, v79, vcc
	v_cmp_lt_i32_e32 vcc, 55, v190
	s_nop 1
	v_cndmask_b32_e32 v80, v161, v80, vcc
	v_cmp_lt_i32_e32 vcc, 56, v190
	s_nop 1
	v_cndmask_b32_e32 v81, v161, v81, vcc
	v_cmp_lt_i32_e32 vcc, 57, v190
	s_nop 1
	v_cndmask_b32_e32 v82, v161, v82, vcc
	v_cmp_lt_i32_e32 vcc, 58, v190
	s_nop 1
	v_cndmask_b32_e32 v83, v161, v83, vcc

; #define VM_WAIT() asm volatile("s_waitcnt vmcnt(0)" ::: "memory")
; #define BAR() do { asm volatile("" ::: "memory"); __builtin_amdgcn_s_barrier(); asm volatile("" ::: "memory"); } while (0)
; #define DMA(ti, slot) do { const int _b = __builtin_amdgcn_readfirstlane(list[ti]); int offK[2], offV[2]; dma_offsets(ldk, wid, lane, offK, offV); \
;         dma_tile(K_lds + (slot) * SHM, Kb, (size_t)_b * 64 * ldk, offK, wid); dma_tile(V_lds + (slot) * SHM, Vb, (size_t)_b * 64 * ldk, offV, wid); } while (0)
; template <int MODE> ...
;     ...
;     DMA(0, 0); if (n > 1) DMA(1, 1); if (n > 2) DMA(2, 2);
;     VM_WAIT(); __syncthreads();
;     if (half) BAR();
;     bf16x8 pa0, pa1, pa2, pa3;
;     int buf = 0;
;     for (int i = 0; i < n; ++i) {
;         const int bcur = __builtin_amdgcn_readfirstlane(list[i]);
;         const int pslot = (buf == 0) ? 2 : buf - 1;
;         const int nslot = (buf == 2) ? 0 : buf + 1;
;         if (half == 0 && i + 1 >= 3 && i + 1 < n) DMA(i + 1, nslot);
.LBB0_828:
	s_barrier
	v_add_f32_e32 v2, v2, v84
	v_add_f32_e32 v179, v179, v2
	s_cmp_eq_u32 s31, 2
	s_mov_b32 s96, 2
	s_cbranch_scc1 .LBB0_849
	s_mov_b32 s13, 2
	v_readlane_b32 s97, v245, 47
	s_mov_b32 s72, 2
	v_mov_b32_e32 v211, s97
	v_add_u32_e32 v211, -8, v211
	ds_read_b32 v208, v211
	ds_read_b32 v209, v211 offset:4
	ds_read_b32 v210, v211 offset:8
.LBB0_830:
	s_add_i32 s12, s13, 1
	s_cmp_lg_u32 s13, 2
	s_cselect_b32 s96, s12, 0
	s_and_b64 vcc, exec, s[8:9]
	s_waitcnt lgkmcnt(0)
	v_readfirstlane_b32 s12, v208
	s_cbranch_vccnz .LBB0_833
	s_add_i32 s14, s72, 1
	s_cmp_ge_i32 s14, s31
	s_cbranch_scc1 .LBB0_833
	s_lshl_b32 s16, s96, 14
	v_readfirstlane_b32 s14, v209
	s_mul_i32 s18, s14, 0x1e8000
	s_mul_hi_i32 s17, s14, 0x1e8000
	s_add_u32 s14, s94, s18
	s_addc_u32 s15, s2, s17
	s_add_i32 s16, s90, s16
	s_add_i32 m0, s16, 0xc000
	v_lshl_add_u64 v[84:85], v[152:153], 1, s[14:15]
	global_load_lds_dwordx4 v[84:85], off
	s_add_i32 m0, s16, 0xc400
	v_lshl_add_u64 v[84:85], v[156:157], 1, s[14:15]
	s_add_u32 s14, s3, s18
	s_addc_u32 s15, s6, s17
	global_load_lds_dwordx4 v[84:85], off
	v_lshl_add_u64 v[84:85], v[154:155], 1, s[14:15]
	s_mov_b32 m0, s16
	s_nop 0
	global_load_lds_dwordx4 v[84:85], off
	v_lshl_add_u64 v[84:85], v[158:159], 1, s[14:15]
	s_add_i32 m0, s16, 0x400
	s_nop 0
	global_load_lds_dwordx4 v[84:85], off

; #define VM_WAIT() asm volatile("s_waitcnt vmcnt(0)" ::: "memory")
; #define BAR() do { asm volatile("" ::: "memory"); __builtin_amdgcn_s_barrier(); asm volatile("" ::: "memory"); } while (0)
; #define DMA(ti, slot) do { const int _b = __builtin_amdgcn_readfirstlane(list[ti]); int offK[2], offV[2]; dma_offsets(ldk, wid, lane, offK, offV); \
;         dma_tile(K_lds + (slot) * SHM, Kb, (size_t)_b * 64 * ldk, offK, wid); dma_tile(V_lds + (slot) * SHM, Vb, (size_t)_b * 64 * ldk, offV, wid); } while (0)
; template <int MODE> ...
;     ...
;         if (half == 1) VM_WAIT();
;         BAR();
;         if (half == 1 && i + 2 >= 3 && i + 2 < n) DMA(i + 2, pslot);
;         const int dist0 = (MODE == 0) ? (t - 31 - 1024 * bcur - 64 * hi) : (t - 64 * bcur - 4 * hi);
;         float nbl = -slope2 * (float)dist0;
;         if (MODE == 1) { const unsigned mw = selw[bcur >> 5]; if (!((mw >> (bcur & 31)) & 1u)) nbl = -__builtin_inff(); }
; #pragma unroll
;         for (int r = 0; r < 16; ++r) { const float c0 = ks * (float)((r & 3) + 8 * (r >> 2)), c1 = c0 + 32.f * ks; p0[r] = fmaf(slope2, c0, p0[r]); p1[r] = fmaf(slope2, c1, p1[r]); }
;         if (bcur >= bA || bcur == bB) {
;             const float base = (float)dist0;
; #pragma unroll
;             for (int r = 0; r < 16; ++r) { const float c0 = ks * (float)((r & 3) + 8 * (r >> 2)), c1 = c0 + 32.f * ks; const float d0 = base - c0, d1 = base - c1;
;                 bool v0 = d0 >= 0.f, v1 = d1 >= 0.f;
;                 if (MODE == 2) { v0 = v0 && (d0 < 512.f); v1 = v1 && (d1 < 512.f); }
;                 p0[r] = v0 ? p0[r] : -__builtin_inff(); p1[r] = v1 ? p1[r] : -__builtin_inff(); }
;         }
.LBB0_835:
	s_setprio 0
	s_barrier
	s_and_b64 vcc, exec, s[10:11]
	s_cbranch_vccnz .LBB0_838
	s_add_i32 s13, s72, 2
	s_cmp_ge_i32 s13, s31
	s_cbranch_scc1 .LBB0_838
	v_readfirstlane_b32 s13, v210
	s_mul_hi_i32 s15, s13, 0x1e8000
	s_mul_i32 s13, s13, 0x1e8000
	s_add_u32 s16, s94, s13
	s_addc_u32 s17, s2, s15
	s_add_i32 s18, s90, s14
	s_add_i32 m0, s18, 0xc000
	v_lshl_add_u64 v[186:187], v[152:153], 1, s[16:17]
	global_load_lds_dwordx4 v[186:187], off
	s_add_i32 m0, s18, 0xc400
	s_add_u32 s14, s3, s13
	v_lshl_add_u64 v[186:187], v[156:157], 1, s[16:17]
	s_addc_u32 s15, s6, s15
	global_load_lds_dwordx4 v[186:187], off
	v_lshl_add_u64 v[186:187], v[154:155], 1, s[14:15]
	s_mov_b32 m0, s18
	s_nop 0
	global_load_lds_dwordx4 v[186:187], off
	v_lshl_add_u64 v[186:187], v[158:159], 1, s[14:15]
	s_add_i32 m0, s18, 0x400
	s_nop 0
	global_load_lds_dwordx4 v[186:187], off
.LBB0_838:
	v_mov_b32_e32 v211, s97
	v_add_u32_e32 v211, -4, v211
	ds_read_b32 v208, v211
	ds_read_b32 v209, v211 offset:4
	ds_read_b32 v210, v211 offset:8
	s_mov_b32 s84, s60
	s_nop 3
	v_fma_f32 v186, 2.0, v134, v70
	v_mov_b32_e32 v70, v71
	v_mov_b32_e32 v71, v72
	s_mov_b32 s14, s23
	s_mov_b32 s15, s56
	v_fma_f32 v187, 0, v134, v68
	v_add_f32_e32 v185, v134, v69
	v_pk_fma_f32 v[68:69], v[134:135], s[84:85], v[84:85]
	v_pk_fma_f32 v[84:85], v[134:135], s[24:25], v[86:87]
	v_pk_fma_f32 v[86:87], v[134:135], s[14:15], v[70:71]
	v_mov_b32_e32 v72, v73
	v_mov_b32_e32 v73, v74
	s_mov_b32 s14, s57
	s_mov_b32 s15, s28
	v_pk_fma_f32 v[70:71], v[134:135], s[26:27], v[88:89]
	v_pk_fma_f32 v[88:89], v[134:135], s[14:15], v[72:73]
	v_mov_b32_e32 v74, v75
	v_mov_b32_e32 v75, v76
	s_mov_b32 s14, s29
	s_mov_b32 s15, s65
	v_pk_fma_f32 v[72:73], v[134:135], s[36:37], v[90:91]
	v_pk_fma_f32 v[90:91], v[134:135], s[14:15], v[74:75]
	s_mov_b32 s74, s61
	v_mov_b32_e32 v76, v77
	v_mov_b32_e32 v77, v78
	s_mov_b32 s14, s95
	s_mov_b32 s15, s38
	v_lshl_add_u32 v2, s12, 6, v140
	v_pk_fma_f32 v[74:75], v[134:135], s[74:75], v[92:93]
	v_pk_fma_f32 v[92:93], v[134:135], s[14:15], v[76:77]
	v_mov_b32_e32 v78, v79
	v_mov_b32_e32 v79, v80
	s_mov_b32 s14, s39
	s_mov_b32 s15, s42
	v_sub_u32_e32 v188, v166, v2
	v_pk_fma_f32 v[76:77], v[134:135], s[40:41], v[94:95]
	v_pk_fma_f32 v[94:95], v[134:135], s[14:15], v[78:79]
	v_mov_b32_e32 v80, v81
	v_mov_b32_e32 v81, v82
	s_mov_b32 s14, s43
	s_mov_b32 s15, s46
	s_cmp_lt_i32 s12, s67
	v_cvt_f32_i32_e32 v2, v188
	v_pk_fma_f32 v[78:79], v[134:135], s[44:45], v[96:97]
	v_pk_fma_f32 v[96:97], v[134:135], s[14:15], v[80:81]
	s_cselect_b64 s[14:15], -1, 0
	s_cmp_lg_u32 s12, s7
	s_cselect_b64 s[12:13], -1, 0
	s_and_b64 s[12:13], s[14:15], s[12:13]
	v_fmac_f32_e32 v83, 0x41d80000, v134
	v_pk_fma_f32 v[80:81], v[134:135], s[48:49], v[98:99]
	s_and_b64 vcc, exec, s[12:13]
	s_cbranch_vccnz .LBB0_840
	s_mov_b32 s12, 0xc2000000
	s_mov_b32 s13, 0xc2040000
	v_pk_add_f32 v[98:99], v[2:3], s[12:13] op_sel_hi:[0,1]
	s_movk_i32 s12, 0x200
	v_cmp_gt_u32_e32 vcc, s12, v188
	s_mov_b32 s12, -1.0
	s_mov_b32 s13, -2.0
	v_pk_add_f32 v[188:189], v[2:3], s[12:13] op_sel_hi:[0,1]
	s_mov_b32 s12, 0xc2080000
	v_cndmask_b32_e32 v187, v161, v187, vcc
	s_mov_b32 s13, 0xc20c0000
	v_cmp_le_f32_e32 vcc, 0, v188
	v_cmp_gt_f32_e64 s[14:15], s82, v188
	v_pk_add_f32 v[190:191], v[2:3], s[12:13] op_sel_hi:[0,1]
	v_cmp_le_f32_e64 s[12:13], 0, v189
	v_cmp_gt_f32_e64 s[16:17], s82, v189
	s_and_b64 vcc, vcc, s[14:15]
	v_cndmask_b32_e32 v185, v161, v185, vcc
	s_and_b64 vcc, s[12:13], s[16:17]
	s_mov_b32 s12, 0xc0400000
	s_mov_b32 s13, 0xc1000000
	v_pk_add_f32 v[188:189], v[2:3], s[12:13] op_sel_hi:[0,1]
	s_mov_b32 s12, 0xc2200000
	v_cndmask_b32_e32 v186, v161, v186, vcc
	s_mov_b32 s13, 0xc2240000
	v_cmp_le_f32_e32 vcc, 0, v188
	v_cmp_gt_f32_e64 s[14:15], s82, v188
	v_pk_add_f32 v[192:193], v[2:3], s[12:13] op_sel_hi:[0,1]
	v_cmp_le_f32_e64 s[12:13], 0, v189
	v_cmp_gt_f32_e64 s[16:17], s82, v189
	s_and_b64 vcc, vcc, s[14:15]
	v_cndmask_b32_e32 v86, v161, v86, vcc
	s_and_b64 vcc, s[12:13], s[16:17]
	s_mov_b32 s12, 0xc1100000
	s_mov_b32 s13, 0xc1200000
	v_pk_add_f32 v[188:189], v[2:3], s[12:13] op_sel_hi:[0,1]
	s_mov_b32 s12, 0xc2280000
	v_cndmask_b32_e32 v87, v161, v87, vcc
	s_mov_b32 s13, 0xc22c0000
	v_cmp_le_f32_e32 vcc, 0, v188
	v_cmp_gt_f32_e64 s[14:15], s82, v188
	v_pk_add_f32 v[196:197], v[2:3], s[12:13] op_sel_hi:[0,1]
	v_cmp_le_f32_e64 s[12:13], 0, v189
	v_cmp_gt_f32_e64 s[16:17], s82, v189
	s_and_b64 vcc, vcc, s[14:15]
	v_cndmask_b32_e32 v88, v161, v88, vcc
	s_and_b64 vcc, s[12:13], s[16:17]
	s_mov_b32 s12, 0xc1300000
	s_mov_b32 s13, 0xc1800000
	v_pk_add_f32 v[188:189], v[2:3], s[12:13] op_sel_hi:[0,1]
	s_mov_b32 s12, 0xc2400000
	v_cndmask_b32_e32 v89, v161, v89, vcc
	s_mov_b32 s13, 0xc2440000
	v_cmp_le_f32_e32 vcc, 0, v188
	v_cmp_gt_f32_e64 s[14:15], s82, v188
	v_pk_add_f32 v[198:199], v[2:3], s[12:13] op_sel_hi:[0,1]
	v_cmp_le_f32_e64 s[12:13], 0, v189
	v_cmp_gt_f32_e64 s[16:17], s82, v189
	s_and_b64 vcc, vcc, s[14:15]
	v_cndmask_b32_e32 v90, v161, v90, vcc
	s_and_b64 vcc, s[12:13], s[16:17]
	s_mov_b32 s12, 0xc1880000
	s_mov_b32 s13, 0xc1900000
; template <int MODE> ...
;     ...
;         if (bcur >= bA || bcur == bB) {
;             const float base = (float)dist0;
; #pragma unroll
;             for (int r = 0; r < 16; ++r) { const float c0 = ks * (float)((r & 3) + 8 * (r >> 2)), c1 = c0 + 32.f * ks; const float d0 = base - c0, d1 = base - c1;
;                 bool v0 = d0 >= 0.f, v1 = d1 >= 0.f;
;                 if (MODE == 2) { v0 = v0 && (d0 < 512.f); v1 = v1 && (d1 < 512.f); }
;                 p0[r] = v0 ? p0[r] : -__builtin_inff(); p1[r] = v1 ? p1[r] : -__builtin_inff(); }
;         }
	v_pk_add_f32 v[188:189], v[2:3], s[12:13] op_sel_hi:[0,1]
	s_mov_b32 s12, 0xc2480000
	v_cndmask_b32_e32 v91, v161, v91, vcc
	s_mov_b32 s13, 0xc24c0000
	v_cmp_le_f32_e32 vcc, 0, v188
	v_cmp_gt_f32_e64 s[14:15], s82, v188
	v_pk_add_f32 v[200:201], v[2:3], s[12:13] op_sel_hi:[0,1]
	v_cmp_le_f32_e64 s[12:13], 0, v189
	v_cmp_gt_f32_e64 s[16:17], s82, v189
	s_and_b64 vcc, vcc, s[14:15]
	v_cndmask_b32_e32 v92, v161, v92, vcc
	s_and_b64 vcc, s[12:13], s[16:17]
	s_mov_b32 s12, 0xc1980000
	s_mov_b32 s13, 0xc1c00000
	v_pk_add_f32 v[188:189], v[2:3], s[12:13] op_sel_hi:[0,1]
	s_mov_b32 s12, 0xc2600000
	v_cndmask_b32_e32 v93, v161, v93, vcc
	s_mov_b32 s13, 0xc2640000
	v_cmp_le_f32_e32 vcc, 0, v188
	v_cmp_gt_f32_e64 s[14:15], s82, v188
	v_pk_add_f32 v[202:203], v[2:3], s[12:13] op_sel_hi:[0,1]
	v_cmp_le_f32_e64 s[12:13], 0, v189
	v_cmp_gt_f32_e64 s[16:17], s82, v189
	s_and_b64 vcc, vcc, s[14:15]
	v_cndmask_b32_e32 v94, v161, v94, vcc
	s_and_b64 vcc, s[12:13], s[16:17]
	s_mov_b32 s12, 0xc1c80000
	s_mov_b32 s13, 0xc1d00000
	v_pk_add_f32 v[188:189], v[2:3], s[12:13] op_sel_hi:[0,1]
	s_mov_b32 s12, 0xc2680000
	v_cndmask_b32_e32 v95, v161, v95, vcc
	s_mov_b32 s13, 0xc26c0000
	v_cmp_le_f32_e32 vcc, 0, v188
	v_cmp_gt_f32_e64 s[14:15], s82, v188
	v_pk_add_f32 v[204:205], v[2:3], s[12:13] op_sel_hi:[0,1]
	v_cmp_le_f32_e64 s[12:13], 0, v189
	v_cmp_gt_f32_e64 s[16:17], s82, v189
	s_and_b64 vcc, vcc, s[14:15]
	v_cmp_le_f32_e64 s[14:15], 0, v190
	v_cmp_gt_f32_e64 s[48:49], s82, v190
	v_cndmask_b32_e32 v96, v161, v96, vcc
	s_and_b64 vcc, s[12:13], s[16:17]
	v_add_f32_e32 v82, 0xc1d80000, v2
	v_cmp_le_f32_e64 s[16:17], 0, v191
	v_cmp_gt_f32_e64 s[50:51], s82, v191
	s_and_b64 s[14:15], s[14:15], s[48:49]
	v_cndmask_b32_e32 v97, v161, v97, vcc
	v_cmp_le_f32_e32 vcc, 0, v82
	v_cmp_gt_f32_e64 s[12:13], s82, v82
	v_cmp_le_f32_e64 s[18:19], 0, v192
	v_cmp_gt_f32_e64 s[52:53], s82, v192
	v_cndmask_b32_e64 v84, v161, v84, s[14:15]
	s_and_b64 s[14:15], s[16:17], s[50:51]
	s_and_b64 vcc, vcc, s[12:13]
	v_cmp_le_f32_e64 s[20:21], 0, v193
	v_cmp_gt_f32_e64 s[54:55], s82, v193
	v_cndmask_b32_e64 v85, v161, v85, s[14:15]
	s_and_b64 s[14:15], s[18:19], s[52:53]
	v_cndmask_b32_e32 v83, v161, v83, vcc
	v_cmp_le_f32_e32 vcc, 0, v98
	v_cmp_le_f32_e64 s[22:23], 0, v196
	v_cmp_gt_f32_e64 s[44:45], s82, v98
	v_cmp_gt_f32_e64 s[56:57], s82, v196
	v_cndmask_b32_e64 v70, v161, v70, s[14:15]
	s_and_b64 s[14:15], s[20:21], s[54:55]
	v_cmp_le_f32_e64 s[24:25], 0, v197
	v_cmp_gt_f32_e64 s[58:59], s82, v197
	s_and_b64 vcc, vcc, s[44:45]
	v_cndmask_b32_e64 v71, v161, v71, s[14:15]
	s_and_b64 s[14:15], s[22:23], s[56:57]
	v_cmp_le_f32_e64 s[12:13], 0, v99
	v_cmp_le_f32_e64 s[26:27], 0, v198
	v_cmp_le_f32_e64 s[36:37], 0, v202
	v_cmp_gt_f32_e64 s[46:47], s82, v99
	v_cmp_gt_f32_e64 s[60:61], s82, v198
	v_cndmask_b32_e32 v68, v161, v68, vcc
	v_cmp_gt_f32_e32 vcc, s82, v202
	v_cndmask_b32_e64 v72, v161, v72, s[14:15]
	s_and_b64 s[14:15], s[24:25], s[58:59]
	v_cmp_le_f32_e64 s[28:29], 0, v199
	v_cmp_le_f32_e64 s[38:39], 0, v203
	v_cmp_gt_f32_e64 s[62:63], s82, v199
	s_and_b64 s[12:13], s[12:13], s[46:47]
	v_cmp_gt_f32_e64 s[46:47], s82, v203
	v_cndmask_b32_e64 v73, v161, v73, s[14:15]
	s_and_b64 s[14:15], s[26:27], s[60:61]
	s_and_b64 vcc, s[36:37], vcc
	v_cmp_le_f32_e64 s[30:31], 0, v200
	v_cmp_le_f32_e64 s[40:41], 0, v204
	v_cmp_gt_f32_e64 s[64:65], s82, v200
	v_cndmask_b32_e64 v69, v161, v69, s[12:13]
	v_cmp_gt_f32_e64 s[12:13], s82, v204
	v_cndmask_b32_e64 v74, v161, v74, s[14:15]
	s_and_b64 s[14:15], s[28:29], s[62:63]
	v_cndmask_b32_e32 v78, v161, v78, vcc
	s_and_b64 vcc, s[38:39], s[46:47]
	v_cmp_le_f32_e64 s[34:35], 0, v201
	v_cmp_le_f32_e64 s[42:43], 0, v205
	v_cmp_gt_f32_e64 s[44:45], s82, v201
	v_cmp_gt_f32_e64 s[48:49], s82, v205
	v_cndmask_b32_e64 v75, v161, v75, s[14:15]
	s_and_b64 s[14:15], s[30:31], s[64:65]
	v_cndmask_b32_e32 v79, v161, v79, vcc
	s_and_b64 vcc, s[40:41], s[12:13]
	v_readlane_b32 s50, v245, 61
	s_mov_b32 s56, 0x41000000
	s_mov_b32 s58, 0x44480000
	s_mov_b32 s60, 0x42000000
	s_mov_b32 s62, 0x43900000
	s_mov_b32 s64, 0
	v_cndmask_b32_e64 v76, v161, v76, s[14:15]
	s_and_b64 s[14:15], s[34:35], s[44:45]
	s_mov_b32 s44, 0x42600000
	s_mov_b32 s38, 0x41900000
	s_mov_b32 s36, 0x42280000
	s_mov_b32 s28, 0x41200000
	s_mov_b32 s26, 0x42200000
	s_mov_b32 s24, 0x42080000
	s_mov_b32 s22, 2.0
	s_mov_b32 s40, 0x42480000
	v_cndmask_b32_e32 v80, v161, v80, vcc
	s_and_b64 vcc, s[42:43], s[48:49]
	s_mov_b32 s48, 0x42680000
	s_mov_b32 s42, 0x41c00000
	v_readlane_b32 s51, v245, 62
	s_mov_b32 s57, 0x41100000
	s_mov_b32 s59, 0x444c0000
	s_mov_b32 s61, 0x42400000
	s_mov_b32 s63, 0x43980000
	v_readlane_b32 s31, v245, 58
	s_mov_b32 s65, 0x41800000
	s_mov_b32 s45, 0x42640000
	v_cndmask_b32_e64 v77, v161, v77, s[14:15]
	s_mov_b32 s46, 0x41d00000
	s_mov_b32 s39, 0x41980000
	s_mov_b32 s37, 0x422c0000
	s_mov_b32 s29, 0x41300000
	s_mov_b32 s27, 0x42240000
	s_mov_b32 s25, 0x420c0000
	s_mov_b32 s23, 0x40400000
	s_mov_b32 s41, 0x424c0000
	s_mov_b32 s49, 0x426c0000
	s_mov_b32 s43, 0x41c80000
	v_cndmask_b32_e32 v81, v161, v81, vcc
	s_mov_b32 s47, 0x41d80000
